# dilated attention: output/lse stores of an item held in registers and issued after the next item's barrier (or at loop exit) so they do not gate the next item's fill and q wait
# baseline (speedup 1.0000x reference)
.LBB0_228:
	s_mov_b32 s50, 0
	v_readlane_b32 s0, v254, 58
	v_readlane_b32 s1, v254, 59
	s_xor_b64 s[0:1], s[0:1], -1
	s_nop 0
	v_cndmask_b32_e64 v0, 0, 1, s[0:1]
	v_cmp_ne_u32_e64 s[2:3], 1, v0
	s_nop 1
	v_writelane_b32 v254, s2, 63
	s_nop 1
	v_writelane_b32 v255, s3, 0
	v_writelane_b32 v255, s0, 1
	s_andn2_b64 vcc, exec, s[0:1]
	s_nop 0
	v_writelane_b32 v255, s1, 2
	s_mov_b64 s[0:1], -1
	s_cbranch_vccnz .LBB0_335
	v_readlane_b32 s0, v254, 62
	s_add_i32 s2, s0, 4
	s_cmp_le_i32 s74, s2
	s_cselect_b64 s[0:1], -1, 0
	s_cmp_lt_i32 s2, s75
	s_cselect_b64 s[2:3], -1, 0
	s_and_b64 s[8:9], s[0:1], s[2:3]
	s_andn2_b64 vcc, exec, s[8:9]
	s_cbranch_vccnz .LBB0_273
	v_readlane_b32 s0, v254, 41
	s_nop 1
	v_mov_b32_e32 v0, s0
	v_readlane_b32 s0, v253, 3
	s_waitcnt vmcnt(0)
	ds_read_b64 v[2:3], v0
	v_readlane_b32 s1, v253, 4
	s_load_dword s2, s[0:1], 0x0
	v_readlane_b32 s0, v253, 0
	v_mbcnt_lo_u32_b32 v0, -1, 0
	v_mbcnt_hi_u32_b32 v0, -1, v0
	s_waitcnt lgkmcnt(0)
	v_readfirstlane_b32 s14, v2
	v_readfirstlane_b32 s15, v3
	v_add_u32_e32 v155, s0, v0
	v_readlane_b32 s0, v253, 56
	v_readlane_b32 s1, v253, 57
	s_and_b64 vcc, exec, s[0:1]
	v_readfirstlane_b32 s3, v155
	s_cbranch_vccz .LBB0_232
	v_readlane_b32 s0, v254, 31
	s_add_u32 s0, s14, s0
	v_readlane_b32 s1, v254, 30
	s_addc_u32 s1, s15, s1
	v_readlane_b32 s12, v254, 38
	v_readlane_b32 s13, v254, 39
	s_add_u32 s0, s0, s12
	s_addc_u32 s1, s1, s13
	v_readlane_b32 s11, v254, 40
	s_add_u32 s0, s0, s11
	v_mov_b32_e32 v8, v155
	s_addc_u32 s1, s1, 0
	s_add_u32 s0, s0, 0xe020800
	v_lshlrev_b32_e32 v0, 4, v8
	s_addc_u32 s1, s1, 0
	v_and_b32_e32 v0, 0x70, v0
	v_lshl_add_u64 v[2:3], s[0:1], 0, v[0:1]
	v_ashrrev_i32_e32 v0, 3, v8
	v_readlane_b32 s17, v253, 61
	v_readlane_b32 s11, v253, 59
	v_readlane_b32 s16, v253, 60
	v_add_u32_e32 v0, s17, v0
	v_max_i32_e32 v0, 0, v0
	v_lshlrev_b32_e32 v0, s11, v0
	v_add_u32_e32 v0, s16, v0
	s_movk_i32 s18, 0x4800
	v_add_u32_e32 v9, 0x200, v8
	v_mad_u64_u32 v[4:5], s[12:13], v0, s18, v[2:3]
	v_ashrrev_i32_e32 v0, 3, v9
	v_add_u32_e32 v0, s17, v0
	v_max_i32_e32 v0, 0, v0
	v_lshlrev_b32_e32 v0, s11, v0
	v_add_u32_e32 v0, s16, v0
	v_mad_u64_u32 v[6:7], s[12:13], v0, s18, v[2:3]
	v_add_u32_e32 v0, 0x400, v8
	v_ashrrev_i32_e32 v0, 3, v0
	v_add_u32_e32 v0, s17, v0
	v_max_i32_e32 v0, 0, v0
	v_lshlrev_b32_e32 v0, s11, v0
	v_add_u32_e32 v0, s16, v0
	global_load_dwordx4 v[106:109], v[4:5], off
	global_load_dwordx4 v[98:101], v[6:7], off
	v_mad_u64_u32 v[4:5], s[12:13], v0, s18, v[2:3]
	v_add_u32_e32 v0, 0x600, v8
	v_ashrrev_i32_e32 v0, 3, v0
	v_add_u32_e32 v0, s17, v0
	v_max_i32_e32 v0, 0, v0
	v_lshlrev_b32_e32 v0, s11, v0
	v_add_u32_e32 v0, s16, v0
	v_mad_u64_u32 v[6:7], s[12:13], v0, s18, v[2:3]
	v_add_u32_e32 v0, 0x800, v8
	v_ashrrev_i32_e32 v0, 3, v0
	v_add_u32_e32 v0, s17, v0
	v_max_i32_e32 v0, 0, v0
	v_lshlrev_b32_e32 v0, s11, v0
	v_add_u32_e32 v0, s16, v0
	global_load_dwordx4 v[114:117], v[4:5], off
	global_load_dwordx4 v[102:105], v[6:7], off
	v_mad_u64_u32 v[4:5], s[12:13], v0, s18, v[2:3]
	v_add_u32_e32 v0, 0xa00, v8
	v_ashrrev_i32_e32 v0, 3, v0
	v_add_u32_e32 v0, s17, v0
	v_max_i32_e32 v0, 0, v0
	v_lshlrev_b32_e32 v0, s11, v0
	v_add_u32_e32 v0, s16, v0
	v_mad_u64_u32 v[2:3], s[12:13], v0, s18, v[2:3]
	s_movk_i32 s12, 0x300
	v_add_u32_e32 v0, 0xfffffe00, v8
	v_cmp_gt_i32_e32 vcc, s12, v8
	global_load_dwordx4 v[118:121], v[4:5], off
	global_load_dwordx4 v[110:113], v[2:3], off
	v_cndmask_b32_e32 v0, v0, v8, vcc
	v_ashrrev_i32_e32 v2, 1, v0
	v_and_b32_e32 v2, -4, v2
	v_add_u32_e32 v2, s17, v2
	v_lshlrev_b32_e32 v0, 4, v0
	v_max_i32_e32 v10, 0, v2
	v_and_b32_e32 v0, 0x70, v0
	v_lshl_add_u64 v[2:3], s[0:1], 0, v[0:1]
	v_lshlrev_b32_e32 v0, s11, v10
	v_add_u32_e32 v0, s16, v0
	v_mad_u64_u32 v[4:5], s[12:13], v0, s18, v[2:3]
	v_add_lshl_u32 v0, v10, 1, s11
	v_add_u32_e32 v0, s16, v0
	v_mad_u64_u32 v[6:7], s[12:13], v0, s18, v[2:3]
	v_add_lshl_u32 v0, v10, 2, s11
	v_add_u32_e32 v0, s16, v0
	global_load_dwordx4 v[82:85], v[4:5], off offset:2048
	global_load_dwordx4 v[86:89], v[6:7], off offset:2048
	v_mad_u64_u32 v[4:5], s[12:13], v0, s18, v[2:3]
	v_add_lshl_u32 v0, v10, 3, s11
	v_add_u32_e32 v0, s16, v0
	v_mad_u64_u32 v[2:3], s[12:13], v0, s18, v[2:3]
	s_movk_i32 s12, 0x100
	s_nop 0
	v_cmp_gt_i32_e32 vcc, s12, v8
	global_load_dwordx4 v[90:93], v[4:5], off offset:2048
	global_load_dwordx4 v[94:97], v[2:3], off offset:2048
	v_cndmask_b32_e32 v0, v8, v9, vcc
	v_ashrrev_i32_e32 v2, 1, v0
	v_and_b32_e32 v2, -4, v2
	v_add_u32_e32 v2, s17, v2
	v_lshlrev_b32_e32 v0, 4, v0
	v_max_i32_e32 v8, 0, v2
	v_and_b32_e32 v0, 0x70, v0
	v_lshl_add_u64 v[2:3], s[0:1], 0, v[0:1]
	v_lshlrev_b32_e32 v0, s11, v8
	v_add_u32_e32 v0, s16, v0
	v_mad_u64_u32 v[4:5], s[0:1], v0, s18, v[2:3]
	v_add_lshl_u32 v0, v8, 1, s11
	v_add_u32_e32 v0, s16, v0
	v_mad_u64_u32 v[6:7], s[0:1], v0, s18, v[2:3]
	v_add_lshl_u32 v0, v8, 2, s11
	v_add_u32_e32 v0, s16, v0
	global_load_dwordx4 v[66:69], v[4:5], off offset:2048
	global_load_dwordx4 v[70:73], v[6:7], off offset:2048
	v_mad_u64_u32 v[4:5], s[0:1], v0, s18, v[2:3]
	v_add_lshl_u32 v0, v8, 3, s11
	v_add_u32_e32 v0, s16, v0
	v_mad_u64_u32 v[2:3], s[0:1], v0, s18, v[2:3]
	global_load_dwordx4 v[74:77], v[4:5], off offset:2048
	global_load_dwordx4 v[78:81], v[2:3], off offset:2048

.LBB0_251:
	s_or_b64 exec, exec, s[0:1]
	s_mul_hi_i32 s0, s33, 0x2aaaaaab
	s_lshr_b32 s1, s0, 31
	s_ashr_i32 s0, s0, 4
	s_add_i32 s25, s0, s1
	s_and_b32 s31, s25, 15
	s_add_i32 s0, s31, 1
	v_cvt_f32_ubyte0_e32 v24, s0
	v_mul_f32_e32 v18, -0.5, v24
	s_mov_b32 s0, 0xc2fc0000
	v_cmp_gt_f32_e32 vcc, s0, v18
	s_and_b64 s[0:1], vcc, exec
	s_cselect_b32 s36, 0xffffffc0, 0
	s_and_b64 s[0:1], s[16:17], exec
	s_cselect_b32 s16, 4, 16
	s_and_b64 s[0:1], s[18:19], exec
	s_cselect_b32 s19, 1, s16
	s_add_i32 s15, s15, s3
	s_lshl_b32 s0, s25, 9
	v_add_u32_e32 v30, s15, v160
	s_and_b32 s0, s0, 0xffffe000
	v_lshlrev_b32_e32 v18, s34, v30
	s_or_b32 s0, s35, s0
	v_add_u32_e32 v158, s0, v18
	v_mov_b64_e32 v[18:19], s[12:13]
	s_movk_i32 s39, 0x4800
	v_mad_i64_i32 v[18:19], s[0:1], v158, s39, v[18:19]
	s_mul_i32 s0, s14, 0xc00
	s_ashr_i32 s1, s0, 31
	s_lshl_b32 s56, s31, 7
	s_add_i32 s18, s33, s2
	s_cmpk_gt_i32 s18, 0xbff
	v_lshl_add_u64 v[18:19], s[0:1], 1, v[18:19]
	s_cselect_b64 s[0:1], -1, 0
	s_cmpk_lt_i32 s18, 0xc00
	s_cselect_b32 s16, s18, s33
	s_ashr_i32 s17, s16, 5
	s_mul_hi_i32 s25, s17, 0x55555556
	s_lshr_b32 s33, s25, 31
	s_add_i32 s25, s25, s33
	s_mul_i32 s25, s25, 3
	s_sub_i32 s17, s17, s25
	s_mul_hi_i32 s25, s16, 0x2aaaaaab
	s_lshr_b32 s33, s25, 31
	s_ashr_i32 s25, s25, 4
	s_add_i32 s25, s25, s33
	s_cmp_eq_u32 s17, 1
	s_cselect_b32 s33, 2, 4
	s_cmp_lg_u32 s17, 0
	s_cselect_b32 s33, s33, 0
	s_lshl_b32 s16, s16, 8
	s_and_b32 s16, s16, 0x1f00
	s_sub_i32 s34, 13, s33
	s_lshr_b32 s37, s16, s34
	s_lshl_b32 s34, s37, s34
	s_sub_i32 s16, s16, s34
	s_add_i32 s38, s16, 0xffffff80
	s_lshl_b32 s16, s25, 9
	s_and_b32 s16, s16, 0xffffe000
	s_mul_hi_i32 s34, s16, 0x4800
	s_mulk_i32 s16, 0x4800
	s_add_u32 s35, s12, s16
	s_mul_i32 s16, s17, 0xc00
	v_lshl_add_u64 v[18:19], v[18:19], 0, s[56:57]
	s_addc_u32 s34, s13, s34
	s_ashr_i32 s17, s16, 31
	v_lshl_add_u64 v[18:19], v[18:19], 0, v[0:1]
	v_mov_b32_e32 v26, v155
	s_lshl_b64 s[16:17], s[16:17], 1
	s_waitcnt vmcnt(0) lgkmcnt(0)
	s_barrier
	s_cmp_eq_u32 s50, 0
	s_cbranch_scc1 .Ldst_skip_n
	global_store_dwordx4 v[208:209], v[192:195], off
	global_store_dwordx4 v[208:209], v[196:199], off offset:32
	global_store_dwordx4 v[208:209], v[200:203], off offset:64
	global_store_dwordx4 v[208:209], v[204:207], off offset:96
	s_mov_b64 s[52:53], exec
	s_and_b64 exec, exec, s[40:41]
	global_store_dword v[210:211], v218, off
	s_mov_b64 exec, s[52:53]
	s_mov_b32 s50, 0
.Ldst_skip_n:
	s_add_u32 s16, s35, s16
	v_add_u32_e32 v27, 0x200, v26
	s_addc_u32 s17, s34, s17
	s_lshl_b32 s25, s25, 7
	v_ashrrev_i32_e32 v20, 3, v26
	v_ashrrev_i32_e32 v22, 3, v27
	s_and_b32 s25, s25, 0x780
	v_add_u32_e32 v20, s38, v20
	v_add_u32_e32 v22, s38, v22
	s_add_u32 s34, s16, s25
	v_lshlrev_b32_e32 v18, 4, v26
	v_max_i32_e32 v20, 0, v20
	v_max_i32_e32 v22, 0, v22
	s_addc_u32 s35, s17, 0
	v_and_b32_e32 v18, 0x70, v18
	v_mov_b32_e32 v19, v1
	v_lshlrev_b32_e32 v20, s33, v20
	v_lshlrev_b32_e32 v22, s33, v22
	s_add_u32 s16, s34, 0x800
	v_lshl_add_u64 v[18:19], s[34:35], 0, v[18:19]
	v_add_u32_e32 v20, s37, v20
	v_add_u32_e32 v22, s37, v22
	s_addc_u32 s17, s35, 0
	v_mad_u64_u32 v[20:21], s[34:35], v20, s39, v[18:19]
	v_mad_u64_u32 v[22:23], s[34:35], v22, s39, v[18:19]
	global_load_dwordx4 v[106:109], v[20:21], off offset:2048
	global_load_dwordx4 v[98:101], v[22:23], off offset:2048
	v_add_u32_e32 v20, 0x400, v26
	v_add_u32_e32 v22, 0x600, v26
	v_ashrrev_i32_e32 v20, 3, v20
	v_ashrrev_i32_e32 v22, 3, v22
	v_add_u32_e32 v20, s38, v20
	v_add_u32_e32 v22, s38, v22
	v_max_i32_e32 v20, 0, v20
	v_max_i32_e32 v22, 0, v22
	v_lshlrev_b32_e32 v20, s33, v20
	v_lshlrev_b32_e32 v22, s33, v22
	v_add_u32_e32 v20, s37, v20
	v_add_u32_e32 v22, s37, v22
	v_mad_u64_u32 v[20:21], s[34:35], v20, s39, v[18:19]
	v_mad_u64_u32 v[22:23], s[34:35], v22, s39, v[18:19]
	global_load_dwordx4 v[114:117], v[20:21], off offset:2048
	global_load_dwordx4 v[102:105], v[22:23], off offset:2048
	v_add_u32_e32 v20, 0x800, v26
	v_add_u32_e32 v22, 0xa00, v26
	v_ashrrev_i32_e32 v20, 3, v20
	v_ashrrev_i32_e32 v22, 3, v22
	v_add_u32_e32 v20, s38, v20
	v_add_u32_e32 v22, s38, v22
	v_max_i32_e32 v20, 0, v20
	v_max_i32_e32 v22, 0, v22
	v_lshlrev_b32_e32 v20, s33, v20
	v_lshlrev_b32_e32 v22, s33, v22
	v_add_u32_e32 v20, s37, v20
	v_add_u32_e32 v22, s37, v22
	v_mad_u64_u32 v[20:21], s[34:35], v20, s39, v[18:19]
	v_mad_u64_u32 v[18:19], s[34:35], v22, s39, v[18:19]
	s_movk_i32 s25, 0x300
	v_cndmask_b32_e32 v25, 0, v224, vcc
	global_load_dwordx4 v[118:121], v[20:21], off offset:2048
	global_load_dwordx4 v[110:113], v[18:19], off offset:2048
	v_add_u32_e32 v18, 0xfffffe00, v26
	v_cmp_gt_i32_e32 vcc, s25, v26
	s_movk_i32 s25, 0x100
	v_fmac_f32_e32 v25, -0.5, v24
	v_cndmask_b32_e32 v18, v18, v26, vcc
	v_ashrrev_i32_e32 v19, 1, v18
	v_and_b32_e32 v19, -4, v19
	v_add_u32_e32 v19, s38, v19
	v_max_i32_e32 v28, 0, v19
	v_lshlrev_b32_e32 v18, 4, v18
	v_and_b32_e32 v18, 0x70, v18
	v_mov_b32_e32 v19, v1
	v_lshlrev_b32_e32 v20, s33, v28
	v_add_lshl_u32 v22, v28, 1, s33
	v_lshl_add_u64 v[18:19], s[16:17], 0, v[18:19]
	v_add_u32_e32 v20, s37, v20
	v_add_u32_e32 v22, s37, v22
	v_mad_u64_u32 v[20:21], s[34:35], v20, s39, v[18:19]
	v_mad_u64_u32 v[22:23], s[34:35], v22, s39, v[18:19]
	global_load_dwordx4 v[82:85], v[20:21], off offset:2048
	global_load_dwordx4 v[86:89], v[22:23], off offset:2048
	v_add_lshl_u32 v20, v28, 2, s33
	v_add_lshl_u32 v22, v28, 3, s33
	v_add_u32_e32 v20, s37, v20
	v_add_u32_e32 v22, s37, v22
	v_mad_u64_u32 v[20:21], s[34:35], v20, s39, v[18:19]
	v_mad_u64_u32 v[18:19], s[34:35], v22, s39, v[18:19]
	v_cmp_gt_i32_e32 vcc, s25, v26
	global_load_dwordx4 v[90:93], v[20:21], off offset:2048
	global_load_dwordx4 v[94:97], v[18:19], off offset:2048
	v_cndmask_b32_e32 v18, v26, v27, vcc
	v_ashrrev_i32_e32 v19, 1, v18
	v_and_b32_e32 v19, -4, v19
	v_add_u32_e32 v19, s38, v19
	v_max_i32_e32 v26, 0, v19
	v_lshlrev_b32_e32 v18, 4, v18
	v_and_b32_e32 v18, 0x70, v18
	v_mov_b32_e32 v19, v1
	v_lshlrev_b32_e32 v20, s33, v26
	v_lshl_add_u64 v[18:19], s[16:17], 0, v[18:19]
	v_add_u32_e32 v20, s37, v20
	v_add_lshl_u32 v22, v26, 1, s33
	v_mad_u64_u32 v[20:21], s[16:17], v20, s39, v[18:19]
	v_add_u32_e32 v22, s37, v22
	v_mad_u64_u32 v[22:23], s[16:17], v22, s39, v[18:19]
	global_load_dwordx4 v[66:69], v[20:21], off offset:2048
	global_load_dwordx4 v[70:73], v[22:23], off offset:2048
	v_add_lshl_u32 v20, v26, 2, s33
	v_add_u32_e32 v20, s37, v20
	v_add_lshl_u32 v22, v26, 3, s33
	v_mad_u64_u32 v[20:21], s[16:17], v20, s39, v[18:19]
	v_add_u32_e32 v22, s37, v22
	v_mad_u64_u32 v[18:19], s[16:17], v22, s39, v[18:19]
	global_load_dwordx4 v[74:77], v[20:21], off offset:2048
	global_load_dwordx4 v[78:81], v[18:19], off offset:2048
	ds_read_b128 v[18:21], v162
	v_exp_f32_e32 v22, v25
	v_cvt_f32_ubyte0_e32 v23, s19
	s_sub_i32 s16, 0x80, s15
	s_ashr_i32 s16, s16, 5
	v_ldexp_f32 v22, v22, s36
	v_mul_f32_e32 v22, 0x3fb8aa3b, v22
	v_mul_f32_e32 v157, v22, v23
	ds_read_b128 v[22:25], v162 offset:32
	s_waitcnt lgkmcnt(1)
	v_mfma_f32_32x32x16_bf16 v[50:65], v[18:21], v[134:137], 0
	ds_read_b128 v[18:21], v162 offset:64
	ds_read_b128 v[26:29], v162 offset:96
	s_cmpk_lt_i32 s15, 0x80
	s_cselect_b32 s17, s16, 0
	s_cmp_gt_i32 s17, 4
	v_sub_u32_e32 v188, v30, v154
	s_waitcnt lgkmcnt(2)
	v_mfma_f32_32x32x16_bf16 v[50:65], v[22:25], v[130:133], v[50:65]
	s_waitcnt lgkmcnt(1)
	v_mfma_f32_32x32x16_bf16 v[50:65], v[18:21], v[126:129], v[50:65]
	s_waitcnt lgkmcnt(0)
	v_mfma_f32_32x32x16_bf16 v[50:65], v[26:29], v[122:125], v[50:65]
	s_cbranch_scc1 .LBB0_260
	s_cmp_eq_u32 s17, 4
	s_cbranch_scc1 .LBB0_254
	ds_read_b128 v[2:5], v163
	ds_read_b128 v[18:21], v163 offset:32
	s_waitcnt lgkmcnt(1)
	v_mfma_f32_32x32x16_bf16 v[2:17], v[2:5], v[134:137], 0
	s_waitcnt lgkmcnt(0)
	v_mfma_f32_32x32x16_bf16 v[2:17], v[18:21], v[130:133], v[2:17]
	ds_read_b128 v[18:21], v163 offset:64
	s_waitcnt lgkmcnt(0)
	v_mfma_f32_32x32x16_bf16 v[2:17], v[18:21], v[126:129], v[2:17]
	ds_read_b128 v[18:21], v163 offset:96
	s_waitcnt lgkmcnt(0)
	v_mfma_f32_32x32x16_bf16 v[2:17], v[18:21], v[122:125], v[2:17]

.LBB0_271:
	ds_bpermute_b32 v50, v161, v146
	s_ashr_i32 s15, s14, 31
	v_mov_b32_e32 v157, v1
	s_waitcnt lgkmcnt(0)
	v_add_f32_e32 v50, v146, v50
	v_div_scale_f32 v51, s[34:35], v50, v50, 1.0
	v_rcp_f32_e32 v52, v51
	s_lshl_b64 s[34:35], s[14:15], 25
	s_add_u32 s34, s11, s34
	s_addc_u32 s35, s26, s35
	v_fma_f32 v53, -v51, v52, 1.0
	v_fmac_f32_e32 v52, v53, v52
	v_div_scale_f32 v53, vcc, 1.0, v50, 1.0
	v_mul_f32_e32 v54, v53, v52
	v_fma_f32 v55, -v51, v54, v53
	v_fmac_f32_e32 v54, v55, v52
	v_fma_f32 v51, -v51, v54, v53
	v_div_fmas_f32 v51, v51, v52, v54
	v_lshlrev_b64 v[54:55], 11, v[158:159]
	v_div_fixup_f32 v52, v51, v50, 1.0
	v_lshl_add_u64 v[54:55], s[34:35], 0, v[54:55]
	s_lshl_b32 s56, s16, 1
	v_lshl_add_u64 v[54:55], v[54:55], 0, s[56:57]
	v_lshl_add_u64 v[54:55], v[54:55], 0, v[156:157]
	v_mbcnt_lo_u32_b32 v216, -1, 0
	v_and_b32_e32 v216, 32, v216
	v_lshrrev_b32_e32 v216, 2, v216
	v_mov_b32_e32 v217, 0
	s_nop 0
	v_lshl_add_u64 v[54:55], v[54:55], 0, v[216:217]
	v_pk_mul_f32 v[56:57], v[34:35], v[52:53] op_sel_hi:[1,0]
	v_pk_mul_f32 v[58:59], v[36:37], v[52:53] op_sel_hi:[1,0]
	v_pk_mul_f32 v[60:61], v[38:39], v[52:53] op_sel_hi:[1,0]
	v_pk_mul_f32 v[62:63], v[40:41], v[52:53] op_sel_hi:[1,0]
	v_cvt_pk_bf16_f32 v192, v56, v57
	v_cvt_pk_bf16_f32 v193, v58, v59
	v_cvt_pk_bf16_f32 v194, v60, v61
	v_cvt_pk_bf16_f32 v195, v62, v63
	s_nop 1
	v_permlane32_swap_b32_e32 v192, v194
	v_permlane32_swap_b32_e32 v193, v195
	v_pk_mul_f32 v[56:57], v[42:43], v[52:53] op_sel_hi:[1,0]
	v_pk_mul_f32 v[58:59], v[44:45], v[52:53] op_sel_hi:[1,0]
	v_pk_mul_f32 v[60:61], v[46:47], v[52:53] op_sel_hi:[1,0]
	v_pk_mul_f32 v[62:63], v[48:49], v[52:53] op_sel_hi:[1,0]
	v_cvt_pk_bf16_f32 v196, v56, v57
	v_cvt_pk_bf16_f32 v197, v58, v59
	v_cvt_pk_bf16_f32 v198, v60, v61
	v_cvt_pk_bf16_f32 v199, v62, v63
	s_nop 1
	v_permlane32_swap_b32_e32 v196, v198
	v_permlane32_swap_b32_e32 v197, v199
	v_pk_mul_f32 v[56:57], v[18:19], v[52:53] op_sel_hi:[1,0]
	v_pk_mul_f32 v[58:59], v[20:21], v[52:53] op_sel_hi:[1,0]
	v_pk_mul_f32 v[60:61], v[22:23], v[52:53] op_sel_hi:[1,0]
	v_pk_mul_f32 v[62:63], v[24:25], v[52:53] op_sel_hi:[1,0]
	v_cvt_pk_bf16_f32 v200, v56, v57
	v_cvt_pk_bf16_f32 v201, v58, v59
	v_cvt_pk_bf16_f32 v202, v60, v61
	v_cvt_pk_bf16_f32 v203, v62, v63
	s_nop 1
	v_permlane32_swap_b32_e32 v200, v202
	v_permlane32_swap_b32_e32 v201, v203
	v_pk_mul_f32 v[56:57], v[26:27], v[52:53] op_sel_hi:[1,0]
	v_pk_mul_f32 v[58:59], v[28:29], v[52:53] op_sel_hi:[1,0]
	v_pk_mul_f32 v[60:61], v[30:31], v[52:53] op_sel_hi:[1,0]
	v_pk_mul_f32 v[62:63], v[32:33], v[52:53] op_sel_hi:[1,0]
	v_cvt_pk_bf16_f32 v204, v56, v57
	v_cvt_pk_bf16_f32 v205, v58, v59
	v_cvt_pk_bf16_f32 v206, v60, v61
	v_cvt_pk_bf16_f32 v207, v62, v63
	s_nop 1
	v_permlane32_swap_b32_e32 v204, v206
	v_permlane32_swap_b32_e32 v205, v207
	v_mov_b64_e32 v[208:209], v[54:55]
	s_mov_b32 s50, 1
	s_and_saveexec_b64 s[16:17], s[40:41]
	s_cbranch_execz .LBB0_234
	v_cmp_gt_f32_e32 vcc, s80, v50
	s_mov_b32 s19, 0x3f317217
	s_lshl_b64 s[14:15], s[14:15], 20
	v_cndmask_b32_e64 v18, 0, 32, vcc
	v_ldexp_f32 v18, v50, v18
	v_log_f32_e32 v18, v18
	v_cndmask_b32_e32 v19, 0, v226, vcc
	s_add_u32 s14, s27, s14
	s_addc_u32 s15, s28, s15
	v_mul_f32_e32 v20, 0x3f317217, v18
	v_fma_f32 v20, v18, s19, -v20
	v_fmac_f32_e32 v20, 0x3377d1cf, v18
	s_mov_b32 s19, 0x7f800000
	v_fmac_f32_e32 v20, 0x3f317217, v18
	v_cmp_lt_f32_e64 vcc, |v18|, s19
	s_lshl_b32 s56, s31, 2
	s_nop 0
	v_cndmask_b32_e32 v18, v18, v20, vcc
	v_sub_f32_e32 v20, v18, v19
	v_lshlrev_b64 v[18:19], 6, v[158:159]
	v_lshl_add_u64 v[18:19], s[14:15], 0, v[18:19]
	v_fmac_f32_e32 v20, 0x3f317218, v189
	v_lshl_add_u64 v[18:19], v[18:19], 0, s[56:57]
	v_mov_b64_e32 v[210:211], v[18:19]
	v_mov_b32_e32 v218, v20
	s_branch .LBB0_234
.LBB0_273:
	s_cmp_eq_u32 s50, 0
	s_cbranch_scc1 .Ldst_skip_x
	global_store_dwordx4 v[208:209], v[192:195], off
	global_store_dwordx4 v[208:209], v[196:199], off offset:32
	global_store_dwordx4 v[208:209], v[200:203], off offset:64
	global_store_dwordx4 v[208:209], v[204:207], off offset:96
	s_mov_b64 s[52:53], exec
	s_and_b64 exec, exec, s[40:41]
	global_store_dword v[210:211], v218, off
	s_mov_b64 exec, s[52:53]
	s_mov_b32 s50, 0
